# grid barrier: first workgroup of an XCC to arrive starts an unwaited L2 write-back
# baseline (speedup 1.0000x reference)
; __device__ __forceinline__ unsigned xb_ld(unsigned* p)              { return __hip_atomic_load(p, __ATOMIC_RELAXED, __HIP_MEMORY_SCOPE_AGENT); }
; __device__ __forceinline__ unsigned xb_add(unsigned* p, unsigned v) { return __hip_atomic_fetch_add(p, v, __ATOMIC_RELAXED, __HIP_MEMORY_SCOPE_AGENT); }
; #define XB_SPIN(cond, bar) do { unsigned _sp = 0; while (cond) { __builtin_amdgcn_s_sleep(1); \
;     if ((++_sp & 255u) == 0u) { if (xb_ld(&(bar)[XB_TMO])) break; if (_sp > XB_SPIN_CAP) { atomicAdd(&(bar)[XB_TMO], 1u); break; } } } } while (0)
; __device__ __forceinline__ void xcd_barrier(const XcdBarrier& b, int tid) {
;     asm volatile("s_waitcnt vmcnt(0)" ::: "memory");
;     __syncthreads();
;     if (tid == 0) {
;         unsigned* bar = b.bar;
;         __builtin_amdgcn_s_waitcnt(0);
;         unsigned nloc = b.st[0], nx = b.st[1];
;         if (nloc == 0u) { xcd_barrier_complete(bar, b.x, nloc, nx); b.st[0] = nloc; b.st[1] = nx; }
;         const unsigned old = xb_add(&bar[XB_XSUB(b.x)], 1u);
;         const unsigned gen = old / nloc;
;         if (old + 1u == (gen + 1u) * nloc) {
;             __builtin_amdgcn_fence(__ATOMIC_RELEASE, "agent");
;             asm volatile("s_waitcnt vmcnt(0)" ::: "memory");
;             const unsigned og = xb_add(&bar[XB_TOP], 1u);
;             const unsigned tg = og / nx;
;             if (og + 1u == (tg + 1u) * nx) xb_add(&bar[XB_TOPGEN], 1u);
;             else XB_SPIN(xb_ld(&bar[XB_TOPGEN]) == tg, bar);
;             __builtin_amdgcn_fence(__ATOMIC_ACQUIRE, "agent");
;             xb_add(&bar[XB_XGEN(b.x)], 1u);
;             asm volatile("s_waitcnt vmcnt(0)" ::: "memory");
;         } else {
;             XB_SPIN(xb_ld(&bar[XB_XGEN(b.x)]) == gen, bar);
;             __builtin_amdgcn_fence(__ATOMIC_ACQUIRE, "agent");
;             asm volatile("s_waitcnt vmcnt(0)" ::: "memory");
;         }
.LBB0_105:
	v_readlane_b32 s0, v249, 2
	s_lshl_b32 s0, s0, 8
	v_readlane_b32 s2, v249, 3
	v_readlane_b32 s3, v249, 4
	s_add_u32 s8, s2, s0
	s_addc_u32 s9, s3, 0
	v_mov_b32_e32 v1, 0x1000
	v_mov_b32_e32 v3, 1
	global_atomic_add v3, v1, v3, s[8:9] offset:1024 sc0
	v_cvt_f32_u32_e32 v1, v2
	v_sub_u32_e32 v4, 0, v2
	v_rcp_iflag_f32_e32 v1, v1
	s_nop 0
	v_mul_f32_e32 v1, 0x4f7ffffe, v1
	v_cvt_u32_f32_e32 v1, v1
	v_mul_lo_u32 v4, v4, v1
	v_mul_hi_u32 v4, v1, v4
	v_add_u32_e32 v1, v1, v4
	s_waitcnt vmcnt(0)
	v_mul_hi_u32 v1, v3, v1
	v_mul_lo_u32 v4, v1, v2
	v_sub_u32_e32 v4, v3, v4
	v_add_u32_e32 v5, 1, v1
	v_cmp_ge_u32_e32 vcc, v4, v2
	v_add_u32_e32 v3, 1, v3
	s_nop 0
	v_cndmask_b32_e32 v1, v1, v5, vcc
	v_sub_u32_e32 v5, v4, v2
	v_cndmask_b32_e32 v4, v4, v5, vcc
	v_add_u32_e32 v5, 1, v1
	v_cmp_ge_u32_e32 vcc, v4, v2
	s_nop 1
	v_cndmask_b32_e32 v1, v1, v5, vcc
	v_mul_lo_u32 v4, v2, v1
	v_add_u32_e32 v2, v4, v2
	v_cmp_ne_u32_e32 vcc, v3, v2
	s_and_saveexec_b64 s[0:1], vcc
	s_xor_b64 s[10:11], exec, s[0:1]
	s_cbranch_execz .LBB0_119
	v_add_u32_e32 v5, 1, v4
	v_cmp_eq_u32_e32 vcc, v3, v5
	s_cbranch_vccz .Lfwb_0
	buffer_wbl2 sc1
.Lfwb_0:
	s_waitcnt lgkmcnt(0)
	buffer_inv sc1
	v_mov_b32_e32 v0, 0x7100
	global_load_dword v0, v0, s[84:85] offset:1024 sc1
	s_add_u32 s16, s84, 0x7500
	s_addc_u32 s17, s85, 0
	s_waitcnt vmcnt(0)
	v_cmp_eq_u32_e32 vcc, v0, v1
	s_and_saveexec_b64 s[12:13], vcc
	s_cbranch_execz .LBB0_118
	s_add_u32 s14, s84, 0x4200
	s_addc_u32 s15, s85, 0
	s_mov_b32 s2, 1
	s_mov_b64 s[18:19], 0
	v_mov_b32_e32 v0, 0
	s_branch .LBB0_109

; __device__ __forceinline__ unsigned xb_ld(unsigned* p)              { return __hip_atomic_load(p, __ATOMIC_RELAXED, __HIP_MEMORY_SCOPE_AGENT); }
; __device__ __forceinline__ unsigned xb_add(unsigned* p, unsigned v) { return __hip_atomic_fetch_add(p, v, __ATOMIC_RELAXED, __HIP_MEMORY_SCOPE_AGENT); }
; #define XB_SPIN(cond, bar) do { unsigned _sp = 0; while (cond) { __builtin_amdgcn_s_sleep(1); \
;     if ((++_sp & 255u) == 0u) { if (xb_ld(&(bar)[XB_TMO])) break; if (_sp > XB_SPIN_CAP) { atomicAdd(&(bar)[XB_TMO], 1u); break; } } } } while (0)
; __device__ __forceinline__ void xcd_barrier(const XcdBarrier& b, int tid) {
;     asm volatile("s_waitcnt vmcnt(0)" ::: "memory");
;     __syncthreads();
;     if (tid == 0) {
;         unsigned* bar = b.bar;
;         __builtin_amdgcn_s_waitcnt(0);
;         unsigned nloc = b.st[0], nx = b.st[1];
;         if (nloc == 0u) { xcd_barrier_complete(bar, b.x, nloc, nx); b.st[0] = nloc; b.st[1] = nx; }
;         const unsigned old = xb_add(&bar[XB_XSUB(b.x)], 1u);
;         const unsigned gen = old / nloc;
;         if (old + 1u == (gen + 1u) * nloc) {
;             __builtin_amdgcn_fence(__ATOMIC_RELEASE, "agent");
;             asm volatile("s_waitcnt vmcnt(0)" ::: "memory");
;             const unsigned og = xb_add(&bar[XB_TOP], 1u);
;             const unsigned tg = og / nx;
;             if (og + 1u == (tg + 1u) * nx) xb_add(&bar[XB_TOPGEN], 1u);
;             else XB_SPIN(xb_ld(&bar[XB_TOPGEN]) == tg, bar);
;             __builtin_amdgcn_fence(__ATOMIC_ACQUIRE, "agent");
;             xb_add(&bar[XB_XGEN(b.x)], 1u);
;             asm volatile("s_waitcnt vmcnt(0)" ::: "memory");
;         } else {
;             XB_SPIN(xb_ld(&bar[XB_XGEN(b.x)]) == gen, bar);
;             __builtin_amdgcn_fence(__ATOMIC_ACQUIRE, "agent");
;             asm volatile("s_waitcnt vmcnt(0)" ::: "memory");
;         }
.LBB0_1130:
	v_readlane_b32 s2, v249, 2
	s_lshl_b32 s2, s2, 8
	v_readlane_b32 s6, v249, 3
	v_readlane_b32 s7, v249, 4
	s_add_u32 s6, s6, s2
	s_addc_u32 s7, s7, 0
	v_mov_b32_e32 v1, 0x1000
	v_mov_b32_e32 v3, 1
	v_sub_u32_e32 v4, 0, v2
	global_atomic_add v3, v1, v3, s[6:7] offset:1024 sc0
	v_cvt_f32_u32_e32 v1, v2
	v_rcp_iflag_f32_e32 v1, v1
	s_nop 0
	v_mul_f32_e32 v1, 0x4f7ffffe, v1
	v_cvt_u32_f32_e32 v1, v1
	v_mul_lo_u32 v4, v4, v1
	v_mul_hi_u32 v4, v1, v4
	v_add_u32_e32 v1, v1, v4
	s_waitcnt vmcnt(0)
	v_mul_hi_u32 v1, v3, v1
	v_mul_lo_u32 v4, v1, v2
	v_sub_u32_e32 v4, v3, v4
	v_add_u32_e32 v5, 1, v1
	v_cmp_ge_u32_e32 vcc, v4, v2
	v_add_u32_e32 v3, 1, v3
	s_nop 0
	v_cndmask_b32_e32 v1, v1, v5, vcc
	v_sub_u32_e32 v5, v4, v2
	v_cndmask_b32_e32 v4, v4, v5, vcc
	v_add_u32_e32 v5, 1, v1
	v_cmp_ge_u32_e32 vcc, v4, v2
	s_nop 1
	v_cndmask_b32_e32 v1, v1, v5, vcc
	v_mul_lo_u32 v4, v2, v1
	v_add_u32_e32 v2, v4, v2
	v_cmp_ne_u32_e32 vcc, v3, v2
	s_and_saveexec_b64 s[2:3], vcc
	s_xor_b64 s[16:17], exec, s[2:3]
	s_cbranch_execz .LBB0_1144
	v_add_u32_e32 v5, 1, v4
	v_cmp_eq_u32_e32 vcc, v3, v5
	s_cbranch_vccz .Lfwb_6
	buffer_wbl2 sc1
.Lfwb_6:
	s_waitcnt lgkmcnt(0)
	buffer_inv sc1
	v_mov_b32_e32 v0, 0x7100
	global_load_dword v0, v0, s[84:85] offset:1024 sc1
	s_add_u32 s22, s84, 0x7500
	s_addc_u32 s23, s85, 0
	s_waitcnt vmcnt(0)
	v_cmp_eq_u32_e32 vcc, v0, v1
	s_and_saveexec_b64 s[18:19], vcc
	s_cbranch_execz .LBB0_1143
	s_add_u32 s20, s84, 0x4200
	s_addc_u32 s21, s85, 0
	s_mov_b32 s2, 1
	s_mov_b64 s[24:25], 0
	v_mov_b32_e32 v0, 0
	s_branch .LBB0_1134

; __device__ __forceinline__ unsigned xb_ld(unsigned* p)              { return __hip_atomic_load(p, __ATOMIC_RELAXED, __HIP_MEMORY_SCOPE_AGENT); }
; __device__ __forceinline__ unsigned xb_add(unsigned* p, unsigned v) { return __hip_atomic_fetch_add(p, v, __ATOMIC_RELAXED, __HIP_MEMORY_SCOPE_AGENT); }
; #define XB_SPIN(cond, bar) do { unsigned _sp = 0; while (cond) { __builtin_amdgcn_s_sleep(1); \
;     if ((++_sp & 255u) == 0u) { if (xb_ld(&(bar)[XB_TMO])) break; if (_sp > XB_SPIN_CAP) { atomicAdd(&(bar)[XB_TMO], 1u); break; } } } } while (0)
; __device__ __forceinline__ void xcd_barrier(const XcdBarrier& b, int tid) {
;     asm volatile("s_waitcnt vmcnt(0)" ::: "memory");
;     __syncthreads();
;     if (tid == 0) {
;         unsigned* bar = b.bar;
;         __builtin_amdgcn_s_waitcnt(0);
;         unsigned nloc = b.st[0], nx = b.st[1];
;         if (nloc == 0u) { xcd_barrier_complete(bar, b.x, nloc, nx); b.st[0] = nloc; b.st[1] = nx; }
;         const unsigned old = xb_add(&bar[XB_XSUB(b.x)], 1u);
;         const unsigned gen = old / nloc;
;         if (old + 1u == (gen + 1u) * nloc) {
;             __builtin_amdgcn_fence(__ATOMIC_RELEASE, "agent");
;             asm volatile("s_waitcnt vmcnt(0)" ::: "memory");
;             const unsigned og = xb_add(&bar[XB_TOP], 1u);
;             const unsigned tg = og / nx;
;             if (og + 1u == (tg + 1u) * nx) xb_add(&bar[XB_TOPGEN], 1u);
;             else XB_SPIN(xb_ld(&bar[XB_TOPGEN]) == tg, bar);
;             __builtin_amdgcn_fence(__ATOMIC_ACQUIRE, "agent");
;             xb_add(&bar[XB_XGEN(b.x)], 1u);
;             asm volatile("s_waitcnt vmcnt(0)" ::: "memory");
;         } else {
;             XB_SPIN(xb_ld(&bar[XB_XGEN(b.x)]) == gen, bar);
;             __builtin_amdgcn_fence(__ATOMIC_ACQUIRE, "agent");
;             asm volatile("s_waitcnt vmcnt(0)" ::: "memory");
;         }
.LBB0_1232:
	v_readlane_b32 s2, v249, 2
	s_lshl_b32 s2, s2, 8
	v_readlane_b32 s6, v249, 3
	v_readlane_b32 s7, v249, 4
	s_add_u32 s6, s6, s2
	s_addc_u32 s7, s7, 0
	v_mov_b32_e32 v1, 0x1000
	v_mov_b32_e32 v3, 1
	v_sub_u32_e32 v4, 0, v2
	global_atomic_add v3, v1, v3, s[6:7] offset:1024 sc0
	v_cvt_f32_u32_e32 v1, v2
	v_rcp_iflag_f32_e32 v1, v1
	s_nop 0
	v_mul_f32_e32 v1, 0x4f7ffffe, v1
	v_cvt_u32_f32_e32 v1, v1
	v_mul_lo_u32 v4, v4, v1
	v_mul_hi_u32 v4, v1, v4
	v_add_u32_e32 v1, v1, v4
	s_waitcnt vmcnt(0)
	v_mul_hi_u32 v1, v3, v1
	v_mul_lo_u32 v4, v1, v2
	v_sub_u32_e32 v4, v3, v4
	v_add_u32_e32 v5, 1, v1
	v_cmp_ge_u32_e32 vcc, v4, v2
	v_add_u32_e32 v3, 1, v3
	s_nop 0
	v_cndmask_b32_e32 v1, v1, v5, vcc
	v_sub_u32_e32 v5, v4, v2
	v_cndmask_b32_e32 v4, v4, v5, vcc
	v_add_u32_e32 v5, 1, v1
	v_cmp_ge_u32_e32 vcc, v4, v2
	s_nop 1
	v_cndmask_b32_e32 v1, v1, v5, vcc
	v_mul_lo_u32 v4, v2, v1
	v_add_u32_e32 v2, v4, v2
	v_cmp_ne_u32_e32 vcc, v3, v2
	s_and_saveexec_b64 s[2:3], vcc
	s_xor_b64 s[8:9], exec, s[2:3]
	s_cbranch_execz .LBB0_1246
	v_add_u32_e32 v5, 1, v4
	v_cmp_eq_u32_e32 vcc, v3, v5
	s_cbranch_vccz .Lfwb_7
	buffer_wbl2 sc1
.Lfwb_7:
	s_waitcnt lgkmcnt(0)
	buffer_inv sc1
	v_mov_b32_e32 v0, 0x7100
	global_load_dword v0, v0, s[84:85] offset:1024 sc1
	s_add_u32 s18, s84, 0x7500
	s_addc_u32 s19, s85, 0
	s_waitcnt vmcnt(0)
	v_cmp_eq_u32_e32 vcc, v0, v1
	s_and_saveexec_b64 s[10:11], vcc
	s_cbranch_execz .LBB0_1245
	s_add_u32 s16, s84, 0x4200
	s_addc_u32 s17, s85, 0
	s_mov_b32 s2, 1
	s_mov_b64 s[20:21], 0
	v_mov_b32_e32 v0, 0
	s_branch .LBB0_1236

; __device__ __forceinline__ unsigned xb_ld(unsigned* p)              { return __hip_atomic_load(p, __ATOMIC_RELAXED, __HIP_MEMORY_SCOPE_AGENT); }
; __device__ __forceinline__ unsigned xb_add(unsigned* p, unsigned v) { return __hip_atomic_fetch_add(p, v, __ATOMIC_RELAXED, __HIP_MEMORY_SCOPE_AGENT); }
; #define XB_SPIN(cond, bar) do { unsigned _sp = 0; while (cond) { __builtin_amdgcn_s_sleep(1); \
;     if ((++_sp & 255u) == 0u) { if (xb_ld(&(bar)[XB_TMO])) break; if (_sp > XB_SPIN_CAP) { atomicAdd(&(bar)[XB_TMO], 1u); break; } } } } while (0)
; __device__ __forceinline__ void xcd_barrier(const XcdBarrier& b, int tid) {
;     ...
;         const unsigned old = xb_add(&bar[XB_XSUB(b.x)], 1u);
;         const unsigned gen = old / nloc;
;         if (old + 1u == (gen + 1u) * nloc) {
;             __builtin_amdgcn_fence(__ATOMIC_RELEASE, "agent");
;             asm volatile("s_waitcnt vmcnt(0)" ::: "memory");
;             const unsigned og = xb_add(&bar[XB_TOP], 1u);
;             const unsigned tg = og / nx;
;             if (og + 1u == (tg + 1u) * nx) xb_add(&bar[XB_TOPGEN], 1u);
;             else XB_SPIN(xb_ld(&bar[XB_TOPGEN]) == tg, bar);
;             __builtin_amdgcn_fence(__ATOMIC_ACQUIRE, "agent");
;             xb_add(&bar[XB_XGEN(b.x)], 1u);
;             asm volatile("s_waitcnt vmcnt(0)" ::: "memory");
;         } else {
;             XB_SPIN(xb_ld(&bar[XB_XGEN(b.x)]) == gen, bar);
.LBB0_1298:
	v_readlane_b32 s2, v249, 2
	s_lshl_b32 s2, s2, 8
	v_readlane_b32 s4, v249, 3
	v_readlane_b32 s5, v249, 4
	s_add_u32 s2, s4, s2
	s_addc_u32 s3, s5, 0
	v_mov_b32_e32 v1, 0x1000
	v_mov_b32_e32 v3, 1
	global_atomic_add v3, v1, v3, s[2:3] offset:1024 sc0
	v_cvt_f32_u32_e32 v1, v2
	v_sub_u32_e32 v4, 0, v2
	v_rcp_iflag_f32_e32 v1, v1
	s_nop 0
	v_mul_f32_e32 v1, 0x4f7ffffe, v1
	v_cvt_u32_f32_e32 v1, v1
	v_mul_lo_u32 v4, v4, v1
	v_mul_hi_u32 v4, v1, v4
	v_add_u32_e32 v1, v1, v4
	s_waitcnt vmcnt(0)
	v_mul_hi_u32 v1, v3, v1
	v_mul_lo_u32 v4, v1, v2
	v_sub_u32_e32 v4, v3, v4
	v_add_u32_e32 v5, 1, v1
	v_cmp_ge_u32_e32 vcc, v4, v2
	v_add_u32_e32 v3, 1, v3
	s_nop 0
	v_cndmask_b32_e32 v1, v1, v5, vcc
	v_sub_u32_e32 v5, v4, v2
	v_cndmask_b32_e32 v4, v4, v5, vcc
	v_add_u32_e32 v5, 1, v1
	v_cmp_ge_u32_e32 vcc, v4, v2
	s_nop 1
	v_cndmask_b32_e32 v1, v1, v5, vcc
	v_mul_lo_u32 v4, v2, v1
	v_add_u32_e32 v2, v4, v2
	v_cmp_ne_u32_e32 vcc, v3, v2
	s_and_saveexec_b64 s[4:5], vcc
	s_xor_b64 s[4:5], exec, s[4:5]
	s_cbranch_execz .LBB0_1312
	v_add_u32_e32 v5, 1, v4
	v_cmp_eq_u32_e32 vcc, v3, v5
	s_cbranch_vccz .Lfwb_8
	buffer_wbl2 sc1
.Lfwb_8:
	s_waitcnt lgkmcnt(0)
	buffer_inv sc1
	v_mov_b32_e32 v0, 0x7100
	global_load_dword v0, v0, s[84:85] offset:1024 sc1
	s_add_u32 s10, s84, 0x7500
	s_addc_u32 s11, s85, 0
	s_waitcnt vmcnt(0)
	v_cmp_eq_u32_e32 vcc, v0, v1
	s_and_saveexec_b64 s[6:7], vcc
	s_cbranch_execz .LBB0_1311
	s_add_u32 s8, s84, 0x4200
	s_addc_u32 s9, s85, 0
	s_mov_b32 s22, 1
	s_mov_b64 s[12:13], 0
	v_mov_b32_e32 v0, 0
	s_branch .LBB0_1302
